# restore the zero constant v200-203 after the PEER route phase (route prefetch had reused it; NSA importance buffer init needs zeros)
# speedup vs baseline: 1.0005x; 1.0005x over previous
.LBB0_3024:
	v_mov_b64_e32 v[200:201], 0
	v_mov_b64_e32 v[202:203], 0
	v_readlane_b32 s0, v254, 25
	v_readlane_b32 s4, v254, 4
	s_or_b32 s18, s0, 11
	v_readlane_b32 s7, v254, 7
	s_cmp_lt_i32 s18, s7
	s_cselect_b64 s[0:1], -1, 0
	s_and_b64 s[2:3], s[2:3], s[0:1]
	s_andn2_b64 vcc, exec, s[2:3]
	v_readlane_b32 s5, v254, 5
	v_readlane_b32 s6, v254, 6
	s_cbranch_vccnz .LBB0_3074
	s_waitcnt vmcnt(0)
	s_waitcnt vmcnt(0) lgkmcnt(0)
	s_barrier
	s_mov_b64 s[2:3], exec
	v_readlane_b32 s4, v254, 19
	v_readlane_b32 s5, v254, 20
	s_and_b64 s[4:5], s[2:3], s[4:5]
	s_mov_b64 exec, s[4:5]
	s_cbranch_execz .LBB0_3073
	v_readlane_b32 s4, v254, 10
	s_waitcnt vmcnt(0) expcnt(0) lgkmcnt(0)
	s_nop 0
	v_mov_b32_e32 v1, s4
	ds_read_b32 v7, v1
	v_readlane_b32 s4, v254, 11
	s_waitcnt lgkmcnt(0)
	v_cmp_ne_u32_e32 vcc, 0, v7
	v_mov_b32_e32 v1, s4
	ds_read_b32 v6, v1
	s_cbranch_vccnz .LBB0_3041
	v_readlane_b32 s6, v250, 56
	v_readlane_b32 s7, v250, 57
	s_load_dwordx2 s[4:5], s[6:7], 0x0
	s_nop 0
	s_load_dword s6, s[6:7], 0x8
	s_mov_b32 s11, 1
	s_waitcnt lgkmcnt(0)
	s_mul_i32 s10, s5, s4
	s_mul_i32 s10, s10, s6
	s_branch .LBB0_3029
